# final-norm loop: loop-head vmcnt(0) removed so the next rows' loads issue while the previous stores drain (on top of v82)
# speedup vs baseline: 1.0048x; 1.0048x over previous
.LBB0_1942:
	s_ashr_i32 s3, s2, 31
	v_mov_b32_e32 v24, 0
	s_and_saveexec_b64 s[4:5], s[0:1]
	s_cbranch_execz .LBB0_1944
	s_lshl_b64 s[6:7], s[2:3], 6
	v_lshl_add_u64 v[22:23], v[18:19], 0, s[6:7]
	global_load_dword v24, v[22:23], off
